# attention-hosted fp8 staging: LDS layout lane*16 + column*1024 (4-way instead of 16-way bank conflicts on the quarter writes, conflict-free b128 read-back)
# speedup vs baseline: 1.0058x; 1.0058x over previous
.Latt_cv_wd:
	s_lshr_b32 s100, s53, 8
	s_lshl_b32 s100, s100, 4
	s_add_i32 s100, s100, 16
	s_cmp_lt_u32 s99, s100
	s_cbranch_scc0 .Latt_cv_skip
	v_mul_f32_e32 v232, 0x42000000, v232
	v_mul_f32_e32 v236, 0x42000000, v236
	v_mul_f32_e32 v240, 0x42000000, v240
	v_mul_f32_e32 v244, 0x42000000, v244
	v_mov_b32_e32 v248, 0
	v_cvt_pk_fp8_f32 v248, v232, v236
	v_cvt_pk_fp8_f32 v248, v240, v244 op_sel:[0,0,1]
	v_mul_f32_e32 v233, 0x42000000, v233
	v_mul_f32_e32 v237, 0x42000000, v237
	v_mul_f32_e32 v241, 0x42000000, v241
	v_mul_f32_e32 v245, 0x42000000, v245
	v_mov_b32_e32 v249, 0
	v_cvt_pk_fp8_f32 v249, v233, v237
	v_cvt_pk_fp8_f32 v249, v241, v245 op_sel:[0,0,1]
	v_mul_f32_e32 v234, 0x42000000, v234
	v_mul_f32_e32 v238, 0x42000000, v238
	v_mul_f32_e32 v242, 0x42000000, v242
	v_mul_f32_e32 v246, 0x42000000, v246
	v_mov_b32_e32 v250, 0
	v_cvt_pk_fp8_f32 v250, v234, v238
	v_cvt_pk_fp8_f32 v250, v242, v246 op_sel:[0,0,1]
	v_mul_f32_e32 v235, 0x42000000, v235
	v_mul_f32_e32 v239, 0x42000000, v239
	v_mul_f32_e32 v243, 0x42000000, v243
	v_mul_f32_e32 v247, 0x42000000, v247
	v_mov_b32_e32 v251, 0
	v_cvt_pk_fp8_f32 v251, v235, v239
	v_cvt_pk_fp8_f32 v251, v243, v247 op_sel:[0,0,1]
	v_mbcnt_lo_u32_b32 v253, -1, 0
	v_mbcnt_hi_u32_b32 v253, -1, v253
	v_lshlrev_b32_e32 v252, 4, v253
	s_and_b32 s100, s98, 7
	s_lshl_b32 s100, s100, 12
	s_add_i32 s100, s100, 0x11000
	s_and_b32 s101, s99, 3
	s_lshl_b32 s101, s101, 2
	s_add_i32 s100, s100, s101
	v_add_u32_e32 v252, s100, v252
	ds_write_b32 v252, v248
	ds_write_b32 v252, v249 offset:1024
	ds_write_b32 v252, v250 offset:2048
	ds_write_b32 v252, v251 offset:3072
	s_cmp_eq_u32 s101, 12
	s_cbranch_scc0 .Latt_cv_nostore
	v_add_u32_e32 v252, -12, v252
	s_waitcnt lgkmcnt(0)
	ds_read_b128 v[232:235], v252
	ds_read_b128 v[236:239], v252 offset:1024
	ds_read_b128 v[240:243], v252 offset:2048
	ds_read_b128 v[244:247], v252 offset:3072
	s_lshr_b32 s100, s99, 2
	s_add_i32 s100, s100, 32
	s_lshl_b32 s100, s100, 11
	s_and_b32 s101, s98, 0x7ff
	s_add_i32 s100, s100, s101
	s_sub_i32 s101, s100, 0x10000
	s_lshr_b32 s101, s101, 10
	s_lshl_b32 s101, s101, 22
	v_mov_b32_e32 v248, s101
	s_and_b32 s101, s100, 63
	s_lshl_b32 s101, s101, 16
	v_add_u32_e32 v248, s101, v248
	s_bfe_u32 s101, s100, 0x40006
	s_lshl_b32 s101, s101, 7
	v_add_u32_e32 v248, s101, v248
	v_lshrrev_b32_e32 v249, 3, v253
	v_and_b32_e32 v250, 7, v253
	v_lshl_add_u32 v248, v249, 4, v248
	v_lshl_add_u32 v248, v250, 13, v248
	v_readlane_b32 s100, v254, 48
	v_readlane_b32 s101, v254, 49
	s_add_u32 s100, s100, 0x14d59400
	s_addc_u32 s101, s101, 0
	s_waitcnt lgkmcnt(0)
	global_store_dwordx4 v248, v[232:235], s[100:101] nt
	global_store_dwordx4 v248, v[236:239], s[100:101] offset:2048 nt
	v_add_u32_e32 v249, 0x1000, v248
	global_store_dwordx4 v249, v[240:243], s[100:101] nt
	global_store_dwordx4 v249, v[244:247], s[100:101] offset:2048 nt
